# attention: waves 4-7 start each item one half query tile later (s_sleep 16) so the two waves of a SIMD alternate MFMA and VALU blocks
# baseline (speedup 1.0000x reference)
.Lat_nz:
	v_lshlrev_b32_e32 v108, 16, v20
	v_and_b32_e32 v109, 0xffff0000, v20
	v_lshlrev_b32_e32 v110, 16, v21
	v_and_b32_e32 v111, 0xffff0000, v21
	v_lshlrev_b32_e32 v112, 16, v22
	v_and_b32_e32 v113, 0xffff0000, v22
	v_lshlrev_b32_e32 v114, 16, v23
	v_and_b32_e32 v115, 0xffff0000, v23
	v_lshlrev_b32_e32 v116, 16, v24
	v_and_b32_e32 v117, 0xffff0000, v24
	v_lshlrev_b32_e32 v118, 16, v25
	v_and_b32_e32 v119, 0xffff0000, v25
	v_lshlrev_b32_e32 v120, 16, v26
	v_and_b32_e32 v121, 0xffff0000, v26
	v_lshlrev_b32_e32 v122, 16, v27
	v_and_b32_e32 v123, 0xffff0000, v27
	v_lshlrev_b32_e32 v124, 16, v28
	v_and_b32_e32 v125, 0xffff0000, v28
	v_lshlrev_b32_e32 v126, 16, v29
	v_and_b32_e32 v127, 0xffff0000, v29
	v_lshlrev_b32_e32 v128, 16, v30
	v_and_b32_e32 v129, 0xffff0000, v30
	v_lshlrev_b32_e32 v130, 16, v31
	v_and_b32_e32 v131, 0xffff0000, v31
	v_lshlrev_b32_e32 v132, 16, v32
	v_and_b32_e32 v133, 0xffff0000, v32
	v_lshlrev_b32_e32 v134, 16, v33
	v_and_b32_e32 v135, 0xffff0000, v33
	v_lshlrev_b32_e32 v136, 16, v34
	v_and_b32_e32 v137, 0xffff0000, v34
	v_lshlrev_b32_e32 v138, 16, v35
	v_and_b32_e32 v139, 0xffff0000, v35
	v_pk_mul_f32 v[232:233], v[108:109], v[108:109]
	v_pk_fma_f32 v[232:233], v[110:111], v[110:111], v[232:233]
	v_pk_fma_f32 v[232:233], v[112:113], v[112:113], v[232:233]
	v_pk_fma_f32 v[232:233], v[114:115], v[114:115], v[232:233]
	v_pk_fma_f32 v[232:233], v[116:117], v[116:117], v[232:233]
	v_pk_fma_f32 v[232:233], v[118:119], v[118:119], v[232:233]
	v_pk_fma_f32 v[232:233], v[120:121], v[120:121], v[232:233]
	v_pk_fma_f32 v[232:233], v[122:123], v[122:123], v[232:233]
	v_pk_fma_f32 v[232:233], v[124:125], v[124:125], v[232:233]
	v_pk_fma_f32 v[232:233], v[126:127], v[126:127], v[232:233]
	v_pk_fma_f32 v[232:233], v[128:129], v[128:129], v[232:233]
	v_pk_fma_f32 v[232:233], v[130:131], v[130:131], v[232:233]
	v_pk_fma_f32 v[232:233], v[132:133], v[132:133], v[232:233]
	v_pk_fma_f32 v[232:233], v[134:135], v[134:135], v[232:233]
	v_pk_fma_f32 v[232:233], v[136:137], v[136:137], v[232:233]
	v_pk_fma_f32 v[232:233], v[138:139], v[138:139], v[232:233]
	s_nop 0
	v_add_f32_e32 v232, v232, v233
	s_barrier
	ds_bpermute_b32 v233, v17, v232
	s_waitcnt lgkmcnt(0)
	v_add_f32_e32 v232, v232, v233
	v_mul_f32_e32 v232, 0x3c800000, v232
	v_add_f32_e32 v232, 0x358637bd, v232
	v_rsq_f32_e32 v232, v232
	s_nop 0
	v_mul_f32_e32 v108, v108, v232
	v_mul_f32_e32 v109, v109, v232
	v_mul_f32_e32 v110, v110, v232
	v_mul_f32_e32 v111, v111, v232
	v_mul_f32_e32 v112, v112, v232
	v_mul_f32_e32 v113, v113, v232
	v_mul_f32_e32 v114, v114, v232
	v_mul_f32_e32 v115, v115, v232
	v_mul_f32_e32 v116, v116, v232
	v_mul_f32_e32 v117, v117, v232
	v_mul_f32_e32 v118, v118, v232
	v_mul_f32_e32 v119, v119, v232
	v_mul_f32_e32 v120, v120, v232
	v_mul_f32_e32 v121, v121, v232
	v_mul_f32_e32 v122, v122, v232
	v_mul_f32_e32 v123, v123, v232
	v_mul_f32_e32 v124, v124, v232
	v_mul_f32_e32 v125, v125, v232
	v_mul_f32_e32 v126, v126, v232
	v_mul_f32_e32 v127, v127, v232
	v_mul_f32_e32 v128, v128, v232
	v_mul_f32_e32 v129, v129, v232
	v_mul_f32_e32 v130, v130, v232
	v_mul_f32_e32 v131, v131, v232
	v_mul_f32_e32 v132, v132, v232
	v_mul_f32_e32 v133, v133, v232
	v_mul_f32_e32 v134, v134, v232
	v_mul_f32_e32 v135, v135, v232
	v_mul_f32_e32 v136, v136, v232
	v_mul_f32_e32 v137, v137, v232
	v_mul_f32_e32 v138, v138, v232
	v_mul_f32_e32 v139, v139, v232
	v_mul_f32_e32 v108, v108, v160
	v_mul_f32_e32 v109, v109, v161
	v_mul_f32_e32 v110, v110, v162
	v_mul_f32_e32 v111, v111, v163
	v_mul_f32_e32 v112, v112, v164
	v_mul_f32_e32 v113, v113, v165
	v_mul_f32_e32 v114, v114, v166
	v_mul_f32_e32 v115, v115, v167
	v_mul_f32_e32 v116, v116, v168
	v_mul_f32_e32 v117, v117, v169
	v_mul_f32_e32 v118, v118, v170
	v_mul_f32_e32 v119, v119, v171
	v_mul_f32_e32 v120, v120, v172
	v_mul_f32_e32 v121, v121, v173
	v_mul_f32_e32 v122, v122, v174
	v_mul_f32_e32 v123, v123, v175
	v_mul_f32_e32 v124, v124, v176
	v_mul_f32_e32 v125, v125, v177
	v_mul_f32_e32 v126, v126, v178
	v_mul_f32_e32 v127, v127, v179
	v_mul_f32_e32 v128, v128, v180
	v_mul_f32_e32 v129, v129, v181
	v_mul_f32_e32 v130, v130, v182
	v_mul_f32_e32 v131, v131, v183
	v_mul_f32_e32 v132, v132, v184
	v_mul_f32_e32 v133, v133, v185
	v_mul_f32_e32 v134, v134, v186
	v_mul_f32_e32 v135, v135, v187
	v_mul_f32_e32 v136, v136, v188
	v_mul_f32_e32 v137, v137, v189
	v_mul_f32_e32 v138, v138, v190
	v_mul_f32_e32 v139, v139, v191
	v_cvt_pk_bf16_f32 v20, v108, v109
	v_cvt_pk_bf16_f32 v21, v110, v111
	v_cvt_pk_bf16_f32 v22, v112, v113
	v_cvt_pk_bf16_f32 v23, v114, v115
	v_cvt_pk_bf16_f32 v24, v116, v117
	v_cvt_pk_bf16_f32 v25, v118, v119
	v_cvt_pk_bf16_f32 v26, v120, v121
	v_cvt_pk_bf16_f32 v27, v122, v123
	v_cvt_pk_bf16_f32 v28, v124, v125
	v_cvt_pk_bf16_f32 v29, v126, v127
	v_cvt_pk_bf16_f32 v30, v128, v129
	v_cvt_pk_bf16_f32 v31, v130, v131
	v_cvt_pk_bf16_f32 v32, v132, v133
	v_cvt_pk_bf16_f32 v33, v134, v135
	v_cvt_pk_bf16_f32 v34, v136, v137
	v_cvt_pk_bf16_f32 v35, v138, v139
	ds_write_b128 v4, v[20:23] offset:0
	ds_write_b128 v4, v[24:27] offset:16
	ds_write_b128 v4, v[28:31] offset:32
	ds_write_b128 v4, v[32:35] offset:48
	ds_write_b128 v5, v[36:39] offset:0
	ds_write_b128 v5, v[40:43] offset:128
	ds_write_b128 v5, v[44:47] offset:256
	ds_write_b128 v5, v[48:51] offset:384
	s_lshl_b32 s2, s37, 14
	s_lshl_b32 s3, s36, 7
	s_add_i32 s2, s2, s3
	s_mul_hi_u32 s5, s2, 0x1400
	s_mul_i32 s4, s2, 0x1400
	s_add_u32 s48, s14, s4
	s_addc_u32 s49, s15, s5
	s_lshl_b32 s4, s38, 7
	s_add_i32 s4, s4, 0x400
	s_add_u32 s48, s48, s4
	s_addc_u32 s49, s49, 0
	s_lshr_b32 s5, s2, 20
	s_lshl_b32 s4, s2, 12
	s_add_u32 s50, s30, s4
	s_addc_u32 s51, s31, s5
	s_lshl_b32 s4, s38, 7
	s_add_u32 s50, s50, s4
	s_addc_u32 s51, s51, 0
	s_lshl_b32 s4, s38, 2
	s_load_dword s54, s[26:27], s4
	s_waitcnt lgkmcnt(0)
	s_barrier
	s_cmp_lt_u32 s33, 4
	s_cbranch_scc1 .Lat_nostag
	s_sleep 16
.Lat_nostag:
	global_load_dwordx4 v[92:95], v8, s[48:49]
	global_load_dwordx4 v[96:99], v8, s[48:49] offset:64
	s_add_i32 s39, s34, s91
	s_cmpk_gt_u32 s39, 0x3ff
	s_cbranch_scc1 .Lat_nopf
	s_and_b32 s3, s39, 3
	s_bfe_u32 s4, s39, 0x70002
	s_lshr_b32 s5, s39, 9
	s_lshl_b32 s6, s5, 14
	s_lshl_b32 s7, s4, 7
	s_add_i32 s6, s6, s7
	s_sub_i32 s6, s6, 0x80
	s_mul_i32 s7, s6, 0x1400
	s_ashr_i32 s9, s7, 31
	s_add_u32 s40, s14, s7
	s_addc_u32 s41, s15, s9
	s_lshl_b32 s7, s3, 7
	s_add_u32 s40, s40, s7
	s_addc_u32 s41, s41, 0
	s_lshl_b32 s6, s5, 2
	s_add_i32 s6, s6, s3
	s_lshl_b32 s6, s6, 21
	s_lshl_b32 s7, s4, 8
	s_sub_i32 s7, s7, 0x100
	s_add_i32 s6, s6, s7
	s_ashr_i32 s7, s6, 31
	s_add_u32 s42, s16, s6
	s_addc_u32 s43, s17, s7
	global_load_dwordx4 v[20:23], v6, s[40:41] offset:0
	global_load_dwordx4 v[24:27], v6, s[40:41] offset:16
	global_load_dwordx4 v[28:31], v6, s[40:41] offset:32
	global_load_dwordx4 v[32:35], v6, s[40:41] offset:48
	global_load_dwordx4 v[36:39], v7, s[42:43] offset:0
	global_load_dwordx4 v[40:43], v7, s[42:43] offset:128
	global_load_dwordx4 v[44:47], v7, s[42:43] offset:256
	global_load_dwordx4 v[48:51], v7, s[42:43] offset:384
	s_branch .Lat_pfd
